# baseline (speedup 1.0000x reference)
_Z11prep_kernelPKfS0_S0_S0_Pc:
	s_load_dwordx2 s[4:5], s[0:1], 0x20
	s_load_dwordx2 s[24:25], s[0:1], 0x8
	s_load_dwordx2 s[26:27], s[0:1], 0x0
	s_load_dwordx2 s[28:29], s[0:1], 0x18
	s_load_dwordx2 s[30:31], s[0:1], 0x10
	v_lshl_or_b32 v2, s2, 8, v0
	s_mov_b32 s2, 0x371ff
	v_cmp_lt_i32_e32 vcc, s2, v2
	s_and_saveexec_b64 s[2:3], vcc
	s_xor_b64 s[6:7], exec, s[2:3]
	s_cbranch_execnz .LBB0_3
	s_andn2_saveexec_b64 s[2:3], s[6:7]
	s_cbranch_execnz .LBB0_60

.LBB0_17:
	s_andn2_saveexec_b64 s[10:11], s[10:11]
	s_cbranch_execz .LBB0_21
	v_add_u32_e32 v0, 0xfffc5dc0, v2
	v_mul_u32_u24_e32 v1, 0xaaab, v0
	v_lshrrev_b32_e32 v3, 22, v1
	v_mul_lo_u16_e32 v1, 0x60, v3
	v_sub_u16_e32 v2, v0, v1
	s_movk_i32 s12, 0x55
	v_cmp_gt_u16_e32 vcc, s12, v2
	v_mov_b32_e32 v1, 0
	v_mov_b32_e32 v4, 0
	s_and_saveexec_b64 s[12:13], vcc
	s_cbranch_execz .LBB0_20
	s_waitcnt lgkmcnt(0)
	s_mov_b64 s[14:15], s[30:31]
	v_and_b32_e32 v3, 0xffff, v3
	s_movk_i32 s16, 0x154
	v_lshlrev_b32_e32 v2, 2, v2
	s_waitcnt lgkmcnt(0)
	v_mov_b64_e32 v[4:5], s[14:15]
	v_mad_u64_u32 v[4:5], s[14:15], v3, s16, v[4:5]
	v_mov_b32_e32 v3, 0
	v_lshl_add_u64 v[2:3], v[4:5], 0, v[2:3]
	global_load_dword v4, v[2:3], off

.LBB0_22:
	s_andn2_saveexec_b64 s[10:11], s[2:3]
	s_cbranch_execz .LBB0_40
	v_add_u32_e32 v2, 0xfffc81c0, v2
	v_lshrrev_b32_e32 v1, 7, v2
	v_mul_lo_u16_e32 v3, 0xab, v1
	v_lshrrev_b16_e32 v3, 9, v3
	s_waitcnt lgkmcnt(0)
	s_mov_b64 s[2:3], s[28:29]
	v_mul_lo_u16_e32 v3, 3, v3
	v_sub_u16_e32 v1, v1, v3
	v_and_b32_e32 v4, 31, v0
	v_lshlrev_b16_e32 v1, 5, v1
	v_lshrrev_b32_e32 v5, 2, v2
	v_lshrrev_b32_e32 v0, 3, v0
	v_and_b32_e32 v1, 0xe0, v1
	v_and_b32_e32 v5, 16, v5
	v_and_b32_e32 v0, 4, v0
	v_or3_b32 v6, v5, v0, v1
	s_movk_i32 s12, 0x55
	v_mov_b32_e32 v1, 0
	v_lshlrev_b32_e32 v0, 2, v4
	v_mul_u32_u24_e32 v3, 0xaaab, v2
	v_cmp_gt_u32_e32 vcc, 10, v4
	s_waitcnt lgkmcnt(0)
	v_lshl_add_u64 v[4:5], s[2:3], 0, v[0:1]
	v_cmp_gt_u32_e64 s[2:3], s12, v6
	v_mul_lo_u16_sdwa v3, v3, s12 dst_sel:DWORD dst_unused:UNUSED_PAD src0_sel:BYTE_3 src1_sel:DWORD
	v_mov_b32_e32 v0, 0
	v_mov_b32_e32 v1, 0
	v_mov_b32_e32 v8, 0
	v_mov_b32_e32 v7, 0
	v_mov_b32_e32 v10, 0
	v_mov_b32_e32 v9, 0
	v_mov_b32_e32 v12, 0
	v_mov_b32_e32 v11, 0
	v_mov_b32_e32 v13, v6
	v_cmp_gt_u32_e64 s[2:3], s12, v13
	s_and_b64 s[14:15], vcc, s[2:3]
	s_and_saveexec_b64 s[2:3], s[14:15]
	v_add_u32_e32 v13, v13, v3
	v_mad_u64_u32 v[14:15], s[16:17], v13, 40, v[4:5]
	global_load_dword v0, v[14:15], off
	s_mov_b64 exec, s[2:3]
	v_or_b32_e32 v13, 1, v6
	v_cmp_gt_u32_e64 s[2:3], s12, v13
	s_and_b64 s[14:15], vcc, s[2:3]
	s_and_saveexec_b64 s[2:3], s[14:15]
	v_add_u32_e32 v13, v13, v3
	v_mad_u64_u32 v[14:15], s[16:17], v13, 40, v[4:5]
	global_load_dword v1, v[14:15], off
	s_mov_b64 exec, s[2:3]
	v_or_b32_e32 v13, 2, v6
	v_cmp_gt_u32_e64 s[2:3], s12, v13
	s_and_b64 s[14:15], vcc, s[2:3]
	s_and_saveexec_b64 s[2:3], s[14:15]
	v_add_u32_e32 v13, v13, v3
	v_mad_u64_u32 v[14:15], s[16:17], v13, 40, v[4:5]
	global_load_dword v8, v[14:15], off
	s_mov_b64 exec, s[2:3]
	v_or_b32_e32 v13, 3, v6
	v_cmp_gt_u32_e64 s[2:3], s12, v13
	s_and_b64 s[14:15], vcc, s[2:3]
	s_and_saveexec_b64 s[2:3], s[14:15]
	v_add_u32_e32 v13, v13, v3
	v_mad_u64_u32 v[14:15], s[16:17], v13, 40, v[4:5]
	global_load_dword v7, v[14:15], off
	s_mov_b64 exec, s[2:3]
	v_or_b32_e32 v13, 8, v6
	v_cmp_gt_u32_e64 s[2:3], s12, v13
	s_and_b64 s[14:15], vcc, s[2:3]
	s_and_saveexec_b64 s[2:3], s[14:15]
	v_add_u32_e32 v13, v13, v3
	v_mad_u64_u32 v[14:15], s[16:17], v13, 40, v[4:5]
	global_load_dword v10, v[14:15], off
	s_mov_b64 exec, s[2:3]
	v_or_b32_e32 v13, 9, v6
	v_cmp_gt_u32_e64 s[2:3], s12, v13
	s_and_b64 s[14:15], vcc, s[2:3]
	s_and_saveexec_b64 s[2:3], s[14:15]
	v_add_u32_e32 v13, v13, v3
	v_mad_u64_u32 v[14:15], s[16:17], v13, 40, v[4:5]
	global_load_dword v9, v[14:15], off
	s_mov_b64 exec, s[2:3]
	v_or_b32_e32 v13, 10, v6
	v_cmp_gt_u32_e64 s[2:3], s12, v13
	s_and_b64 s[14:15], vcc, s[2:3]
	s_and_saveexec_b64 s[2:3], s[14:15]
	v_add_u32_e32 v13, v13, v3
	v_mad_u64_u32 v[14:15], s[16:17], v13, 40, v[4:5]
	global_load_dword v12, v[14:15], off
	s_mov_b64 exec, s[2:3]
	v_or_b32_e32 v13, 11, v6
	v_cmp_gt_u32_e64 s[2:3], s12, v13
	s_and_b64 s[14:15], vcc, s[2:3]
	s_and_saveexec_b64 s[2:3], s[14:15]
	v_add_u32_e32 v13, v13, v3
	v_mad_u64_u32 v[14:15], s[16:17], v13, 40, v[4:5]
	global_load_dword v11, v[14:15], off
	s_mov_b64 exec, s[2:3]
	s_waitcnt vmcnt(0)
	v_cvt_f16_f32_e32 v0, v0
	v_cvt_f16_f32_e32 v1, v1
	v_cvt_f16_f32_e32 v8, v8
	v_cvt_f16_f32_e32 v7, v7
	v_cvt_f16_f32_e32 v10, v10
	v_cvt_f16_f32_e32 v9, v9
	v_cvt_f16_f32_e32 v12, v12
	v_cvt_f16_f32_e32 v11, v11

.LBB0_41:
	s_andn2_saveexec_b64 s[2:3], s[8:9]
	s_cbranch_execz .LBB0_59
	s_waitcnt lgkmcnt(0)
	s_mov_b64 s[8:9], s[26:27]
	v_add_u32_e32 v2, 0xfffc8e00, v2
	v_and_b32_e32 v4, 31, v0
	v_lshrrev_b32_e32 v0, 3, v0
	v_and_b32_e32 v0, 4, v0
	v_lshrrev_b32_e32 v1, 2, v2
	s_mov_b32 s10, 0x3ffffff0
	v_cmp_gt_u32_e32 vcc, 24, v4
	v_and_or_b32 v6, v1, s10, v0
	v_mov_b32_e32 v1, 0
	v_mov_b32_e32 v0, 0
	v_mov_b32_e32 v5, 0
	v_mov_b32_e32 v3, 0
	v_mov_b32_e32 v8, 0
	v_mov_b32_e32 v7, 0
	v_mov_b32_e32 v10, 0
	v_mov_b32_e32 v9, 0
	s_and_saveexec_b64 s[10:11], vcc
	v_mul_lo_u32 v11, v6, 24
	v_or_b32_e32 v12, v11, v4
	v_mov_b32_e32 v13, 0
	s_waitcnt lgkmcnt(0)
	v_lshl_add_u64 v[12:13], v[12:13], 2, s[8:9]
	global_load_dword v1, v[12:13], off
	global_load_dword v0, v[12:13], off offset:96
	global_load_dword v5, v[12:13], off offset:192
	global_load_dword v3, v[12:13], off offset:288
	global_load_dword v8, v[12:13], off offset:768
	global_load_dword v7, v[12:13], off offset:864
	global_load_dword v10, v[12:13], off offset:960
	global_load_dword v9, v[12:13], off offset:1056
	s_waitcnt vmcnt(0)
	v_mul_f32_e32 v1, 0x44800000, v1
	v_mul_f32_e32 v0, 0x44800000, v0
	v_mul_f32_e32 v5, 0x44800000, v5
	v_mul_f32_e32 v3, 0x44800000, v3
	v_mul_f32_e32 v8, 0x44800000, v8
	v_mul_f32_e32 v7, 0x44800000, v7
	v_mul_f32_e32 v10, 0x44800000, v10
	v_mul_f32_e32 v9, 0x44800000, v9

	.amdhsa_kernel _Z11prep_kernelPKfS0_S0_S0_Pc
		.amdhsa_group_segment_fixed_size 0
		.amdhsa_private_segment_fixed_size 0
		.amdhsa_kernarg_size 40
		.amdhsa_user_sgpr_count 2
		.amdhsa_user_sgpr_dispatch_ptr 0
		.amdhsa_user_sgpr_queue_ptr 0
		.amdhsa_user_sgpr_kernarg_segment_ptr 1
		.amdhsa_user_sgpr_dispatch_id 0
		.amdhsa_user_sgpr_kernarg_preload_length 0
		.amdhsa_user_sgpr_kernarg_preload_offset 0
		.amdhsa_user_sgpr_private_segment_size 0
		.amdhsa_uses_dynamic_stack 0
		.amdhsa_enable_private_segment 0
		.amdhsa_system_sgpr_workgroup_id_x 1
		.amdhsa_system_sgpr_workgroup_id_y 0
		.amdhsa_system_sgpr_workgroup_id_z 0
		.amdhsa_system_sgpr_workgroup_info 0
		.amdhsa_system_vgpr_workitem_id 0
		.amdhsa_next_free_vgpr 20
		.amdhsa_next_free_sgpr 32
		.amdhsa_accum_offset 20
		.amdhsa_reserve_vcc 1
		.amdhsa_float_round_mode_32 0
		.amdhsa_float_round_mode_16_64 0
		.amdhsa_float_denorm_mode_32 3
		.amdhsa_float_denorm_mode_16_64 3
		.amdhsa_dx10_clamp 1
		.amdhsa_ieee_mode 1
		.amdhsa_fp16_overflow 0
		.amdhsa_tg_split 0
		.amdhsa_exception_fp_ieee_invalid_op 0
		.amdhsa_exception_fp_denorm_src 0
		.amdhsa_exception_fp_ieee_div_zero 0
		.amdhsa_exception_fp_ieee_overflow 0
		.amdhsa_exception_fp_ieee_underflow 0
		.amdhsa_exception_fp_ieee_inexact 0
		.amdhsa_exception_int_div_zero 0
	.end_amdhsa_kernel
